# flattened P1 classes with larger quotas: 5 stolen tiles per GEMM workgroup of class A, 14 tiles per converter workgroup
# baseline (speedup 1.0000x reference)
; #define LAS __attribute__((address_space(3)))
; template <bool STEAL>
; __device__ __forceinline__ void f8_convert(const Args& a, LAS unsigned char* lds, unsigned char* ws, int l, int first, int stride, int quota, unsigned* ticket, int tid, int lane, int wave) {
;     ...
;     while (k < F8_TILES_PER_LAYER) {
;         LAS unsigned char* buf = lds + (n & 1) * 65536;
;         if constexpr (STEAL) { if (tid == 0) word[(n + 1) & 1] = (n + 1 < quota) ? (int)__hip_atomic_fetch_add(ticket, 1u, __ATOMIC_RELAXED, __HIP_MEMORY_SCOPE_AGENT) : F8_TILES_PER_LAYER; }
.LBB0_247:
	s_and_saveexec_b64 s[2:3], s[0:1]
	s_xor_b64 s[2:3], exec, s[2:3]
	s_and_b32 s4, s35, 1
	s_or_saveexec_b64 s[2:3], s[2:3]
	v_mov_b32_e32 v152, s4
	s_xor_b64 exec, exec, s[2:3]
	s_cbranch_execz .LBB0_253
	v_readlane_b32 s4, v255, 61
	s_nop 0
	s_cmp_eq_u32 s4, 3
	s_cselect_b32 s4, 13, 4
	s_cmp_gt_u32 s35, s4
	v_mov_b32_e32 v152, 0x6e0
	s_cbranch_scc1 .LBB0_252
	v_mov_b64_e32 v[152:153], s[6:7]
	flat_atomic_add v152, v[152:153], v206 sc0
